# speedup vs baseline: 1.0040x; 1.0040x over previous
.LBB1_69:
	s_or_b64 exec, exec, s[2:3]
	v_or_b32_e32 v100, v126, v125
	v_add_u32_e32 v104, 16, v100
	v_or_b32_e32 v101, v100, v121
	v_add_u16_e32 v102, v104, v121
	v_lshlrev_b32_e32 v101, 1, v101
	v_lshrrev_b16_e32 v102, 1, v102
	v_and_b32_e32 v101, 0x7fc, v101
	v_lshlrev_b32_e32 v102, 2, v102
	s_waitcnt vmcnt(0)
	s_barrier
	s_movk_i32 s14, 0x60
	v_cmp_gt_u32_e64 s[10:11], s14, v107
	s_and_saveexec_b64 s[12:13], s[10:11]
	s_cbranch_execz .Llb_pf_skip
	v_readlane_b32 s14, v230, 4
	v_readlane_b32 s15, v230, 5
	v_and_b32_e32 v212, -16, v98
	v_mul_u32_u24_e32 v212, 0xc00, v212
	v_add_u32_e32 v212, v212, v239
	s_nop 1
	global_load_dwordx2 v[182:183], v212, s[14:15] sc1
	global_load_dwordx2 v[184:185], v212, s[14:15] offset:3072 sc1
	v_add_u32_e32 v213, 0x1800, v212
	global_load_dwordx2 v[186:187], v213, s[14:15] sc1
	global_load_dwordx2 v[188:189], v213, s[14:15] offset:3072 sc1
	v_add_u32_e32 v213, 0x3000, v212
	global_load_dwordx2 v[190:191], v213, s[14:15] sc1
	global_load_dwordx2 v[192:193], v213, s[14:15] offset:3072 sc1
	v_add_u32_e32 v213, 0x4800, v212
	global_load_dwordx2 v[194:195], v213, s[14:15] sc1
	global_load_dwordx2 v[196:197], v213, s[14:15] offset:3072 sc1
	v_add_u32_e32 v213, 0x6000, v212
	global_load_dwordx2 v[198:199], v213, s[14:15] sc1
	global_load_dwordx2 v[200:201], v213, s[14:15] offset:3072 sc1
	v_add_u32_e32 v213, 0x7800, v212
	global_load_dwordx2 v[202:203], v213, s[14:15] sc1
	global_load_dwordx2 v[204:205], v213, s[14:15] offset:3072 sc1
	v_add_u32_e32 v213, 0x9000, v212
	global_load_dwordx2 v[206:207], v213, s[14:15] sc1
	global_load_dwordx2 v[208:209], v213, s[14:15] offset:3072 sc1
	v_add_u32_e32 v213, 0xa800, v212
	global_load_dwordx2 v[210:211], v213, s[14:15] sc1
.Llb_pf_skip:
	s_mov_b64 exec, s[12:13]
	v_mov_b32_e32 v101, v232
	v_lshrrev_b32_e32 v103, 2, v107
	v_mov_b32_e32 v102, v233
	v_bitop3_b32 v108, v126, v124, v125 bitop3:0x36
	v_and_or_b32 v105, v103, 12, v127
	v_lshlrev_b32_e32 v103, 1, v108
	v_add_u32_e32 v108, 32, v100
	v_add_u16_e32 v113, v108, v121
	v_lshrrev_b16_e32 v113, 1, v113
	v_lshlrev_b32_e32 v113, 2, v113
	v_mov_b32_e32 v113, v234
	v_add_u32_e32 v110, 0x60, v100
	v_add_u32_e32 v111, 0x70, v100
	s_movk_i32 s1, 0x180
	v_or_b32_e32 v112, 0x80, v100
	v_mul_lo_u32 v105, v105, s1
	v_xor_b32_e32 v104, v104, v124
	v_add_u16_e32 v114, v110, v121
	v_add_u16_e32 v115, v111, v121
	v_add_u16_e32 v112, v112, v121
	v_add3_u32 v116, 0, v103, v105
	v_lshlrev_b32_e32 v103, 1, v104
	v_lshrrev_b16_e32 v104, 1, v114
	v_lshrrev_b16_e32 v114, 1, v115
	v_lshrrev_b16_e32 v112, 1, v112
	v_add3_u32 v115, 0, v103, v105
	v_lshlrev_b32_e32 v103, 2, v104
	v_lshlrev_b32_e32 v104, 2, v114
	v_lshlrev_b32_e32 v112, 2, v112
	v_mov_b32_e32 v114, v235
	s_nop 0
	v_mov_b32_e32 v104, v236
	s_nop 0
	v_mov_b32_e32 v103, v237
	v_and_b32_e32 v247, 1, v107
	v_cmp_eq_u32_e64 s[12:13], 0, v247
	v_mov_b32_e32 v245, 0x1000504
	v_mov_b32_e32 v247, 0x5040100
	v_cndmask_b32_e64 v245, v245, v247, s[12:13]
	v_mov_b32_e32 v246, 0x3020706
	v_mov_b32_e32 v247, 0x7060302
	v_cndmask_b32_e64 v246, v246, v247, s[12:13]
	v_lshrrev_b32_e32 v247, 7, v107
	v_lshlrev_b32_e32 v247, 5, v247
	v_bfe_u32 v254, v107, 4, 2
	v_lshl_add_u32 v247, v254, 2, v247
	v_mul_u32_u24_e32 v247, 0x180, v247
	v_mov_b32_e32 v244, 0x2fe
	v_cndmask_b32_e64 v244, v244, 0, s[12:13]
	v_add_u32_e32 v247, v247, v244
	v_lshlrev_b32_e32 v254, 4, v254
	v_bfe_u32 v244, v107, 6, 1
	v_mul_u32_u24_e32 v244, 48, v244
	v_and_b32_e32 v248, 15, v107
	v_add_u32_e32 v244, v244, v248
	v_mov_b32_e32 v248, v244
	v_xor_b32_e32 v248, v248, v254
	v_lshl_add_u32 v248, v248, 1, v247
	v_add_u32_e32 v249, 16, v244
	v_xor_b32_e32 v249, v249, v254
	v_lshl_add_u32 v249, v249, 1, v247
	v_add_u32_e32 v250, 32, v244
	v_xor_b32_e32 v250, v250, v254
	v_lshl_add_u32 v250, v250, 1, v247
	v_add_u32_e32 v251, 96, v244
	v_xor_b32_e32 v251, v251, v254
	v_lshl_add_u32 v251, v251, 1, v247
	v_add_u32_e32 v252, 112, v244
	v_xor_b32_e32 v252, v252, v254
	v_lshl_add_u32 v252, v252, 1, v247
	v_add_u32_e32 v253, 128, v244
	v_xor_b32_e32 v253, v253, v254
	v_lshl_add_u32 v253, v253, 1, v247
	v_fma_mixlo_f16 v82, v82, v232, 0
	v_fma_mixlo_f16 v84, v84, v232, 0
	v_fma_mixlo_f16 v86, v86, v232, 0
	v_fma_mixlo_f16 v88, v88, v232, 0
	v_fma_mixhi_f16 v82, v83, v232, 0
	v_fma_mixhi_f16 v84, v85, v232, 0
	v_fma_mixhi_f16 v86, v87, v232, 0
	v_fma_mixhi_f16 v88, v89, v232, 0
	v_cndmask_b32_e64 v83, v82, v84, s[12:13]
	v_cndmask_b32_e64 v85, v84, v82, s[12:13]
	v_cndmask_b32_e64 v87, v86, v88, s[12:13]
	v_cndmask_b32_e64 v89, v88, v86, s[12:13]
	v_mov_b32_e32 v254, v248
	v_add_u32_e32 v247, 0x1800, v248
	v_mov_b32_dpp v244, v83 quad_perm:[1,0,3,2] row_mask:0xf bank_mask:0xf
	v_mov_b32_dpp v255, v87 quad_perm:[1,0,3,2] row_mask:0xf bank_mask:0xf
	v_perm_b32 v82, v244, v85, v245
	v_perm_b32 v84, v244, v85, v246
	ds_write2_b32 v254, v82, v84 offset1:96
	v_perm_b32 v86, v255, v89, v245
	v_perm_b32 v88, v255, v89, v246
	ds_write2_b32 v247, v86, v88 offset1:96
	v_fma_mixlo_f16 v90, v90, v232, 0
	v_fma_mixlo_f16 v92, v92, v232, 0
	v_fma_mixlo_f16 v94, v94, v232, 0
	v_fma_mixlo_f16 v96, v96, v232, 0
	v_fma_mixhi_f16 v90, v91, v232, 0
	v_fma_mixhi_f16 v92, v93, v232, 0
	v_fma_mixhi_f16 v94, v95, v232, 0
	v_fma_mixhi_f16 v96, v97, v232, 0
	v_cndmask_b32_e64 v91, v90, v92, s[12:13]
	v_cndmask_b32_e64 v93, v92, v90, s[12:13]
	v_cndmask_b32_e64 v95, v94, v96, s[12:13]
	v_cndmask_b32_e64 v97, v96, v94, s[12:13]
	v_add_u32_e32 v254, 0xc000, v248
	v_add_u32_e32 v247, 0xd800, v248
	v_mov_b32_dpp v244, v91 quad_perm:[1,0,3,2] row_mask:0xf bank_mask:0xf
	v_mov_b32_dpp v255, v95 quad_perm:[1,0,3,2] row_mask:0xf bank_mask:0xf
	v_perm_b32 v90, v244, v93, v245
	v_perm_b32 v92, v244, v93, v246
	ds_write2_b32 v254, v90, v92 offset1:96
	v_perm_b32 v94, v255, v97, v245
	v_perm_b32 v96, v255, v97, v246
	ds_write2_b32 v247, v94, v96 offset1:96
	v_fma_mixlo_f16 v70, v70, v233, 0
	v_fma_mixlo_f16 v72, v72, v233, 0
	v_fma_mixlo_f16 v66, v66, v233, 0
	v_fma_mixlo_f16 v68, v68, v233, 0
	v_fma_mixhi_f16 v70, v71, v233, 0
	v_fma_mixhi_f16 v72, v73, v233, 0
	v_fma_mixhi_f16 v66, v67, v233, 0
	v_fma_mixhi_f16 v68, v69, v233, 0
	v_cndmask_b32_e64 v71, v70, v72, s[12:13]
	v_cndmask_b32_e64 v73, v72, v70, s[12:13]
	v_cndmask_b32_e64 v67, v66, v68, s[12:13]
	v_cndmask_b32_e64 v69, v68, v66, s[12:13]
	v_mov_b32_e32 v254, v249
	v_add_u32_e32 v247, 0x1800, v249
	v_mov_b32_dpp v244, v71 quad_perm:[1,0,3,2] row_mask:0xf bank_mask:0xf
	v_mov_b32_dpp v255, v67 quad_perm:[1,0,3,2] row_mask:0xf bank_mask:0xf
	v_perm_b32 v70, v244, v73, v245
	v_perm_b32 v72, v244, v73, v246
	ds_write2_b32 v254, v70, v72 offset1:96
	v_perm_b32 v66, v255, v69, v245
	v_perm_b32 v68, v255, v69, v246
	ds_write2_b32 v247, v66, v68 offset1:96
	v_fma_mixlo_f16 v78, v78, v233, 0
	v_fma_mixlo_f16 v80, v80, v233, 0
	v_fma_mixlo_f16 v74, v74, v233, 0
	v_fma_mixlo_f16 v76, v76, v233, 0
	v_fma_mixhi_f16 v78, v79, v233, 0
	v_fma_mixhi_f16 v80, v81, v233, 0
	v_fma_mixhi_f16 v74, v75, v233, 0
	v_fma_mixhi_f16 v76, v77, v233, 0
	v_cndmask_b32_e64 v79, v78, v80, s[12:13]
	v_cndmask_b32_e64 v81, v80, v78, s[12:13]
	v_cndmask_b32_e64 v75, v74, v76, s[12:13]
	v_cndmask_b32_e64 v77, v76, v74, s[12:13]
	v_add_u32_e32 v254, 0xc000, v249
	v_add_u32_e32 v247, 0xd800, v249
	v_mov_b32_dpp v244, v79 quad_perm:[1,0,3,2] row_mask:0xf bank_mask:0xf
	v_mov_b32_dpp v255, v75 quad_perm:[1,0,3,2] row_mask:0xf bank_mask:0xf
	v_perm_b32 v78, v244, v81, v245
	v_perm_b32 v80, v244, v81, v246
	ds_write2_b32 v254, v78, v80 offset1:96
	v_perm_b32 v74, v255, v77, v245
	v_perm_b32 v76, v255, v77, v246
	ds_write2_b32 v247, v74, v76 offset1:96
	v_fma_mixlo_f16 v46, v46, v234, 0
	v_fma_mixlo_f16 v48, v48, v234, 0
	v_fma_mixlo_f16 v42, v42, v234, 0
	v_fma_mixlo_f16 v44, v44, v234, 0
	v_fma_mixhi_f16 v46, v47, v234, 0
	v_fma_mixhi_f16 v48, v49, v234, 0
	v_fma_mixhi_f16 v42, v43, v234, 0
	v_fma_mixhi_f16 v44, v45, v234, 0
	v_cndmask_b32_e64 v47, v46, v48, s[12:13]
	v_cndmask_b32_e64 v49, v48, v46, s[12:13]
	v_cndmask_b32_e64 v43, v42, v44, s[12:13]
	v_cndmask_b32_e64 v45, v44, v42, s[12:13]
	v_mov_b32_e32 v254, v250
	v_add_u32_e32 v247, 0x1800, v250
	v_mov_b32_dpp v244, v47 quad_perm:[1,0,3,2] row_mask:0xf bank_mask:0xf
	v_mov_b32_dpp v255, v43 quad_perm:[1,0,3,2] row_mask:0xf bank_mask:0xf
	v_perm_b32 v46, v244, v49, v245
	v_perm_b32 v48, v244, v49, v246
	ds_write2_b32 v254, v46, v48 offset1:96
	v_perm_b32 v42, v255, v45, v245
	v_perm_b32 v44, v255, v45, v246
	ds_write2_b32 v247, v42, v44 offset1:96
	v_fma_mixlo_f16 v62, v62, v234, 0
	v_fma_mixlo_f16 v64, v64, v234, 0
	v_fma_mixlo_f16 v58, v58, v234, 0
	v_fma_mixlo_f16 v60, v60, v234, 0
	v_fma_mixhi_f16 v62, v63, v234, 0
	v_fma_mixhi_f16 v64, v65, v234, 0
	v_fma_mixhi_f16 v58, v59, v234, 0
	v_fma_mixhi_f16 v60, v61, v234, 0
	v_cndmask_b32_e64 v63, v62, v64, s[12:13]
	v_cndmask_b32_e64 v65, v64, v62, s[12:13]
	v_cndmask_b32_e64 v59, v58, v60, s[12:13]
	v_cndmask_b32_e64 v61, v60, v58, s[12:13]
	v_add_u32_e32 v254, 0xc000, v250
	v_add_u32_e32 v247, 0xd800, v250
	v_mov_b32_dpp v244, v63 quad_perm:[1,0,3,2] row_mask:0xf bank_mask:0xf
	v_mov_b32_dpp v255, v59 quad_perm:[1,0,3,2] row_mask:0xf bank_mask:0xf
	v_perm_b32 v62, v244, v65, v245
	v_perm_b32 v64, v244, v65, v246
	ds_write2_b32 v254, v62, v64 offset1:96
	v_perm_b32 v58, v255, v61, v245
	v_perm_b32 v60, v255, v61, v246
	ds_write2_b32 v247, v58, v60 offset1:96
	v_fma_mixlo_f16 v38, v38, v235, 0
	v_fma_mixlo_f16 v40, v40, v235, 0
	v_fma_mixlo_f16 v34, v34, v235, 0
	v_fma_mixlo_f16 v36, v36, v235, 0
	v_fma_mixhi_f16 v38, v39, v235, 0
	v_fma_mixhi_f16 v40, v41, v235, 0
	v_fma_mixhi_f16 v34, v35, v235, 0
	v_fma_mixhi_f16 v36, v37, v235, 0
	v_cndmask_b32_e64 v39, v38, v40, s[12:13]
	v_cndmask_b32_e64 v41, v40, v38, s[12:13]
	v_cndmask_b32_e64 v35, v34, v36, s[12:13]
	v_cndmask_b32_e64 v37, v36, v34, s[12:13]
	v_mov_b32_e32 v254, v251
	v_add_u32_e32 v247, 0x1800, v251
	v_mov_b32_dpp v244, v39 quad_perm:[1,0,3,2] row_mask:0xf bank_mask:0xf
	v_mov_b32_dpp v255, v35 quad_perm:[1,0,3,2] row_mask:0xf bank_mask:0xf
	v_perm_b32 v38, v244, v41, v245
	v_perm_b32 v40, v244, v41, v246
	ds_write2_b32 v254, v38, v40 offset1:96
	v_perm_b32 v34, v255, v37, v245
	v_perm_b32 v36, v255, v37, v246
	ds_write2_b32 v247, v34, v36 offset1:96
	v_fma_mixlo_f16 v54, v54, v235, 0
	v_fma_mixlo_f16 v56, v56, v235, 0
	v_fma_mixlo_f16 v50, v50, v235, 0
	v_fma_mixlo_f16 v52, v52, v235, 0
	v_fma_mixhi_f16 v54, v55, v235, 0
	v_fma_mixhi_f16 v56, v57, v235, 0
	v_fma_mixhi_f16 v50, v51, v235, 0
	v_fma_mixhi_f16 v52, v53, v235, 0
	v_cndmask_b32_e64 v55, v54, v56, s[12:13]
	v_cndmask_b32_e64 v57, v56, v54, s[12:13]
	v_cndmask_b32_e64 v51, v50, v52, s[12:13]
	v_cndmask_b32_e64 v53, v52, v50, s[12:13]
	v_add_u32_e32 v254, 0xc000, v251
	v_add_u32_e32 v247, 0xd800, v251
	v_mov_b32_dpp v244, v55 quad_perm:[1,0,3,2] row_mask:0xf bank_mask:0xf
	v_mov_b32_dpp v255, v51 quad_perm:[1,0,3,2] row_mask:0xf bank_mask:0xf
	v_perm_b32 v54, v244, v57, v245
	v_perm_b32 v56, v244, v57, v246
	ds_write2_b32 v254, v54, v56 offset1:96
	v_perm_b32 v50, v255, v53, v245
	v_perm_b32 v52, v255, v53, v246
	ds_write2_b32 v247, v50, v52 offset1:96
	v_fma_mixlo_f16 v22, v22, v236, 0
	v_fma_mixlo_f16 v24, v24, v236, 0
	v_fma_mixlo_f16 v18, v18, v236, 0
	v_fma_mixlo_f16 v20, v20, v236, 0
	v_fma_mixhi_f16 v22, v23, v236, 0
	v_fma_mixhi_f16 v24, v25, v236, 0
	v_fma_mixhi_f16 v18, v19, v236, 0
	v_fma_mixhi_f16 v20, v21, v236, 0
	v_cndmask_b32_e64 v23, v22, v24, s[12:13]
	v_cndmask_b32_e64 v25, v24, v22, s[12:13]
	v_cndmask_b32_e64 v19, v18, v20, s[12:13]
	v_cndmask_b32_e64 v21, v20, v18, s[12:13]
	v_mov_b32_e32 v254, v252
	v_add_u32_e32 v247, 0x1800, v252
	v_mov_b32_dpp v244, v23 quad_perm:[1,0,3,2] row_mask:0xf bank_mask:0xf
	v_mov_b32_dpp v255, v19 quad_perm:[1,0,3,2] row_mask:0xf bank_mask:0xf
	v_perm_b32 v22, v244, v25, v245
	v_perm_b32 v24, v244, v25, v246
	ds_write2_b32 v254, v22, v24 offset1:96
	v_perm_b32 v18, v255, v21, v245
	v_perm_b32 v20, v255, v21, v246
	ds_write2_b32 v247, v18, v20 offset1:96
	v_fma_mixlo_f16 v30, v30, v236, 0
	v_fma_mixlo_f16 v32, v32, v236, 0
	v_fma_mixlo_f16 v26, v26, v236, 0
	v_fma_mixlo_f16 v28, v28, v236, 0
	v_fma_mixhi_f16 v30, v31, v236, 0
	v_fma_mixhi_f16 v32, v33, v236, 0
	v_fma_mixhi_f16 v26, v27, v236, 0
	v_fma_mixhi_f16 v28, v29, v236, 0
	v_cndmask_b32_e64 v31, v30, v32, s[12:13]
	v_cndmask_b32_e64 v33, v32, v30, s[12:13]
	v_cndmask_b32_e64 v27, v26, v28, s[12:13]
	v_cndmask_b32_e64 v29, v28, v26, s[12:13]
	v_add_u32_e32 v254, 0xc000, v252
	v_add_u32_e32 v247, 0xd800, v252
	v_mov_b32_dpp v244, v31 quad_perm:[1,0,3,2] row_mask:0xf bank_mask:0xf
	v_mov_b32_dpp v255, v27 quad_perm:[1,0,3,2] row_mask:0xf bank_mask:0xf
	v_perm_b32 v30, v244, v33, v245
	v_perm_b32 v32, v244, v33, v246
	ds_write2_b32 v254, v30, v32 offset1:96
	v_perm_b32 v26, v255, v29, v245
	v_perm_b32 v28, v255, v29, v246
	ds_write2_b32 v247, v26, v28 offset1:96
	v_fma_mixlo_f16 v6, v6, v237, 0
	v_fma_mixlo_f16 v8, v8, v237, 0
	v_fma_mixlo_f16 v2, v2, v237, 0
	v_fma_mixlo_f16 v4, v4, v237, 0
	v_fma_mixhi_f16 v6, v7, v237, 0
	v_fma_mixhi_f16 v8, v9, v237, 0
	v_fma_mixhi_f16 v2, v3, v237, 0
	v_fma_mixhi_f16 v4, v5, v237, 0
	v_cndmask_b32_e64 v7, v6, v8, s[12:13]
	v_cndmask_b32_e64 v9, v8, v6, s[12:13]
	v_cndmask_b32_e64 v3, v2, v4, s[12:13]
	v_cndmask_b32_e64 v5, v4, v2, s[12:13]
	v_mov_b32_e32 v254, v253
	v_add_u32_e32 v247, 0x1800, v253
	v_mov_b32_dpp v244, v7 quad_perm:[1,0,3,2] row_mask:0xf bank_mask:0xf
	v_mov_b32_dpp v255, v3 quad_perm:[1,0,3,2] row_mask:0xf bank_mask:0xf
	v_perm_b32 v6, v244, v9, v245
	v_perm_b32 v8, v244, v9, v246
	ds_write2_b32 v254, v6, v8 offset1:96
	v_perm_b32 v2, v255, v5, v245
	v_perm_b32 v4, v255, v5, v246
	ds_write2_b32 v247, v2, v4 offset1:96
	v_fma_mixlo_f16 v14, v14, v237, 0
	v_fma_mixlo_f16 v16, v16, v237, 0
	v_fma_mixlo_f16 v10, v10, v237, 0
	v_fma_mixlo_f16 v12, v12, v237, 0
	v_fma_mixhi_f16 v14, v15, v237, 0
	v_fma_mixhi_f16 v16, v17, v237, 0
	v_fma_mixhi_f16 v10, v11, v237, 0
	v_fma_mixhi_f16 v12, v13, v237, 0
	v_cndmask_b32_e64 v15, v14, v16, s[12:13]
	v_cndmask_b32_e64 v17, v16, v14, s[12:13]
	v_cndmask_b32_e64 v11, v10, v12, s[12:13]
	v_cndmask_b32_e64 v13, v12, v10, s[12:13]
	v_add_u32_e32 v254, 0xc000, v253
	v_add_u32_e32 v247, 0xd800, v253
	v_mov_b32_dpp v244, v15 quad_perm:[1,0,3,2] row_mask:0xf bank_mask:0xf
	v_mov_b32_dpp v255, v11 quad_perm:[1,0,3,2] row_mask:0xf bank_mask:0xf
	v_perm_b32 v14, v244, v17, v245
	v_perm_b32 v16, v244, v17, v246
	ds_write2_b32 v254, v14, v16 offset1:96
	v_perm_b32 v10, v255, v13, v245
	v_perm_b32 v12, v255, v13, v246
	ds_write2_b32 v247, v10, v12 offset1:96
	s_movk_i32 s0, 0x80
	v_cmp_gt_i32_e64 s[2:3], s1, v107
	v_xor_b32_e32 v66, v108, v124
	v_lshlrev_b32_e32 v66, 1, v66
	v_add3_u32 v66, 0, v66, v105
	v_xor_b32_e32 v42, v110, v124
	v_lshlrev_b32_e32 v42, 1, v42
	v_add3_u32 v42, 0, v42, v105
	v_xor_b32_e32 v34, v111, v124
	v_lshlrev_b32_e32 v34, 1, v34
	v_add3_u32 v34, 0, v34, v105
	v_bitop3_b32 v18, v100, v124, s0 bitop3:0x36
	v_lshlrev_b32_e32 v18, 1, v18
	v_add3_u32 v18, 0, v18, v105
	s_mov_b32 s0, 0x2aaaaaab
	v_mul_hi_i32 v2, v107, s0
	v_lshrrev_b32_e32 v3, 31, v2
	v_ashrrev_i32_e32 v2, 4, v2
	v_add_u32_e32 v49, v2, v3
	s_movk_i32 s0, 0x60
	v_mul_lo_u32 v2, v49, s0
	v_sub_u32_e32 v14, v107, v2
	v_lshrrev_b32_e32 v2, 1, v121
	s_movk_i32 s0, 0x5e80
	v_add_u32_e32 v8, v14, v2
	v_mov_b32_e32 v7, 0
	v_lshlrev_b32_e32 v2, 2, v14
	v_mul_lo_u32 v3, v49, s0
	v_ashrrev_i32_e32 v9, 31, v8
	v_mul_lo_u32 v45, v49, s75
	v_xor_b32_e32 v48, 0x60, v2
	v_xor_b32_e32 v47, 64, v2
	v_xor_b32_e32 v46, 32, v2
	v_add3_u32 v44, v3, v123, 0
	v_mov_b32_e32 v6, v7
	v_mov_b32_e32 v3, v7
	v_mov_b32_e32 v4, v7
	s_waitcnt lgkmcnt(0)
	s_barrier
	s_and_saveexec_b64 s[0:1], s[2:3]
	s_cbranch_execz .LBB1_73
	v_readlane_b32 s4, v230, 2
	v_readlane_b32 s5, v230, 3
	v_mov_b32_e32 v12, 0
	v_mov_b32_e32 v13, v12
	v_mov_b32_e32 v2, v240
	v_mov_b32_e32 v3, v241
	v_mov_b32_e32 v6, v242
	v_mov_b32_e32 v7, v243
	v_readlane_b32 s4, v230, 10
	v_readlane_b32 s6, v230, 4
	v_readlane_b32 s7, v230, 5
	v_add3_u32 v15, v45, v48, s4
	s_add_i32 s4, 0, 0xc00
	v_add3_u32 v16, v45, v47, s4
	s_add_i32 s4, 0, 0x600
	v_add3_u32 v17, v45, v46, s4
	v_mov_b32_e32 v26, v44
	v_add_u32_e32 v27, 0x200, v44
	v_mov_b32_e32 v28, v17
	v_add_u32_e32 v29, 0x200, v17
	v_mov_b32_e32 v30, v16
	v_add_u32_e32 v31, 0x200, v16
	v_mov_b32_e32 v32, v15
	v_add_u32_e32 v33, 0x200, v15
	ds_read2_b32 v[50:51], v26 offset1:96
	ds_read2_b32 v[52:53], v27 offset0:64 offset1:160
	ds_read2_b32 v[54:55], v28 offset1:96
	ds_read2_b32 v[56:57], v29 offset0:64 offset1:160
	v_add_u32_e32 v26, 0x1800, v26
	v_add_u32_e32 v27, 0x1800, v27
	v_add_u32_e32 v28, 0x1800, v28
	v_add_u32_e32 v29, 0x1800, v29
	ds_read2_b32 v[58:59], v30 offset1:96
	ds_read2_b32 v[60:61], v31 offset0:64 offset1:160
	ds_read2_b32 v[62:63], v32 offset1:96
	ds_read2_b32 v[64:65], v33 offset0:64 offset1:160
	v_add_u32_e32 v30, 0x1800, v30
	v_add_u32_e32 v31, 0x1800, v31
	v_add_u32_e32 v32, 0x1800, v32
	v_add_u32_e32 v33, 0x1800, v33
	ds_read2_b32 v[66:67], v26 offset1:96
	ds_read2_b32 v[68:69], v27 offset0:64 offset1:160
	ds_read2_b32 v[70:71], v28 offset1:96
	ds_read2_b32 v[72:73], v29 offset0:64 offset1:160
	v_add_u32_e32 v26, 0x1800, v26
	v_add_u32_e32 v27, 0x1800, v27
	v_add_u32_e32 v28, 0x1800, v28
	v_add_u32_e32 v29, 0x1800, v29
	v_xor_b32_e32 v4, 0x80000000, v3
	v_mov_b32_e32 v10, v2
	v_mov_b32_e32 v11, v2
	v_mov_b32_e32 v5, v3
	s_waitcnt lgkmcnt(8)
	v_cvt_f32_f16_e32 v74, v50
	v_cvt_f32_f16_sdwa v75, v50 dst_sel:DWORD dst_unused:UNUSED_PAD src0_sel:WORD_1
	v_cvt_f32_f16_e32 v76, v51
	v_cvt_f32_f16_sdwa v77, v51 dst_sel:DWORD dst_unused:UNUSED_PAD src0_sel:WORD_1
	v_cvt_f32_f16_e32 v78, v52
	v_cvt_f32_f16_sdwa v79, v52 dst_sel:DWORD dst_unused:UNUSED_PAD src0_sel:WORD_1
	v_cvt_f32_f16_e32 v80, v53
	v_cvt_f32_f16_sdwa v81, v53 dst_sel:DWORD dst_unused:UNUSED_PAD src0_sel:WORD_1
	v_cvt_f32_f16_e32 v82, v54
	v_cvt_f32_f16_sdwa v83, v54 dst_sel:DWORD dst_unused:UNUSED_PAD src0_sel:WORD_1
	v_cvt_f32_f16_e32 v84, v55
	v_cvt_f32_f16_sdwa v85, v55 dst_sel:DWORD dst_unused:UNUSED_PAD src0_sel:WORD_1
	v_cvt_f32_f16_e32 v86, v56
	v_cvt_f32_f16_sdwa v87, v56 dst_sel:DWORD dst_unused:UNUSED_PAD src0_sel:WORD_1
	v_cvt_f32_f16_e32 v88, v57
	v_cvt_f32_f16_sdwa v89, v57 dst_sel:DWORD dst_unused:UNUSED_PAD src0_sel:WORD_1
	ds_read2_b32 v[50:51], v30 offset1:96
	ds_read2_b32 v[52:53], v31 offset0:64 offset1:160
	ds_read2_b32 v[54:55], v32 offset1:96
	ds_read2_b32 v[56:57], v33 offset0:64 offset1:160
	v_add_u32_e32 v30, 0x1800, v30
	v_add_u32_e32 v31, 0x1800, v31
	v_add_u32_e32 v32, 0x1800, v32
	v_add_u32_e32 v33, 0x1800, v33
	s_waitcnt lgkmcnt(8)
	v_pk_fma_f32 v[74:75], v[4:5], v[12:13], v[74:75] op_sel:[0,1,0] op_sel_hi:[1,0,1]
	v_cvt_f32_f16_e32 v90, v58
	v_pk_fma_f32 v[12:13], v[10:11], v[12:13], v[74:75]
	v_cvt_f32_f16_sdwa v91, v58 dst_sel:DWORD dst_unused:UNUSED_PAD src0_sel:WORD_1
	v_pk_fma_f32 v[76:77], v[4:5], v[12:13], v[76:77] op_sel:[0,1,0] op_sel_hi:[1,0,1]
	v_cvt_f32_f16_e32 v92, v59
	v_pk_fma_f32 v[12:13], v[10:11], v[12:13], v[76:77]
	v_cvt_f32_f16_sdwa v93, v59 dst_sel:DWORD dst_unused:UNUSED_PAD src0_sel:WORD_1
	v_pk_fma_f32 v[78:79], v[4:5], v[12:13], v[78:79] op_sel:[0,1,0] op_sel_hi:[1,0,1]
	v_cvt_f32_f16_e32 v94, v60
	v_pk_fma_f32 v[12:13], v[10:11], v[12:13], v[78:79]
	v_cvt_f32_f16_sdwa v95, v60 dst_sel:DWORD dst_unused:UNUSED_PAD src0_sel:WORD_1
	v_pk_fma_f32 v[80:81], v[4:5], v[12:13], v[80:81] op_sel:[0,1,0] op_sel_hi:[1,0,1]
	v_cvt_f32_f16_e32 v96, v61
	v_pk_fma_f32 v[12:13], v[10:11], v[12:13], v[80:81]
	v_cvt_f32_f16_sdwa v97, v61 dst_sel:DWORD dst_unused:UNUSED_PAD src0_sel:WORD_1
	v_pk_fma_f32 v[82:83], v[4:5], v[12:13], v[82:83] op_sel:[0,1,0] op_sel_hi:[1,0,1]
	v_cvt_f32_f16_e32 v18, v62
	v_pk_fma_f32 v[12:13], v[10:11], v[12:13], v[82:83]
	v_cvt_f32_f16_sdwa v19, v62 dst_sel:DWORD dst_unused:UNUSED_PAD src0_sel:WORD_1
	v_pk_fma_f32 v[84:85], v[4:5], v[12:13], v[84:85] op_sel:[0,1,0] op_sel_hi:[1,0,1]
	v_cvt_f32_f16_e32 v20, v63
	v_pk_fma_f32 v[12:13], v[10:11], v[12:13], v[84:85]
	v_cvt_f32_f16_sdwa v21, v63 dst_sel:DWORD dst_unused:UNUSED_PAD src0_sel:WORD_1
	v_pk_fma_f32 v[86:87], v[4:5], v[12:13], v[86:87] op_sel:[0,1,0] op_sel_hi:[1,0,1]
	v_cvt_f32_f16_e32 v22, v64
	v_pk_fma_f32 v[12:13], v[10:11], v[12:13], v[86:87]
	v_cvt_f32_f16_sdwa v23, v64 dst_sel:DWORD dst_unused:UNUSED_PAD src0_sel:WORD_1
	v_pk_fma_f32 v[88:89], v[4:5], v[12:13], v[88:89] op_sel:[0,1,0] op_sel_hi:[1,0,1]
	v_cvt_f32_f16_e32 v24, v65
	v_pk_fma_f32 v[12:13], v[10:11], v[12:13], v[88:89]
	v_cvt_f32_f16_sdwa v25, v65 dst_sel:DWORD dst_unused:UNUSED_PAD src0_sel:WORD_1
	ds_read2_b32 v[58:59], v26 offset1:96
	ds_read2_b32 v[60:61], v27 offset0:64 offset1:160
	ds_read2_b32 v[62:63], v28 offset1:96
	ds_read2_b32 v[64:65], v29 offset0:64 offset1:160
	v_add_u32_e32 v26, 0x1800, v26
	v_add_u32_e32 v27, 0x1800, v27
	v_add_u32_e32 v28, 0x1800, v28
	v_add_u32_e32 v29, 0x1800, v29
	s_waitcnt lgkmcnt(8)
	v_pk_fma_f32 v[90:91], v[4:5], v[12:13], v[90:91] op_sel:[0,1,0] op_sel_hi:[1,0,1]
	v_cvt_f32_f16_e32 v74, v66
	v_pk_fma_f32 v[12:13], v[10:11], v[12:13], v[90:91]
	v_cvt_f32_f16_sdwa v75, v66 dst_sel:DWORD dst_unused:UNUSED_PAD src0_sel:WORD_1
	v_pk_fma_f32 v[92:93], v[4:5], v[12:13], v[92:93] op_sel:[0,1,0] op_sel_hi:[1,0,1]
	v_cvt_f32_f16_e32 v76, v67
	v_pk_fma_f32 v[12:13], v[10:11], v[12:13], v[92:93]
	v_cvt_f32_f16_sdwa v77, v67 dst_sel:DWORD dst_unused:UNUSED_PAD src0_sel:WORD_1
	v_pk_fma_f32 v[94:95], v[4:5], v[12:13], v[94:95] op_sel:[0,1,0] op_sel_hi:[1,0,1]
	v_cvt_f32_f16_e32 v78, v68
	v_pk_fma_f32 v[12:13], v[10:11], v[12:13], v[94:95]
	v_cvt_f32_f16_sdwa v79, v68 dst_sel:DWORD dst_unused:UNUSED_PAD src0_sel:WORD_1
	v_pk_fma_f32 v[96:97], v[4:5], v[12:13], v[96:97] op_sel:[0,1,0] op_sel_hi:[1,0,1]
	v_cvt_f32_f16_e32 v80, v69
	v_pk_fma_f32 v[12:13], v[10:11], v[12:13], v[96:97]
	v_cvt_f32_f16_sdwa v81, v69 dst_sel:DWORD dst_unused:UNUSED_PAD src0_sel:WORD_1
	v_pk_fma_f32 v[18:19], v[4:5], v[12:13], v[18:19] op_sel:[0,1,0] op_sel_hi:[1,0,1]
	v_cvt_f32_f16_e32 v82, v70
	v_pk_fma_f32 v[12:13], v[10:11], v[12:13], v[18:19]
	v_cvt_f32_f16_sdwa v83, v70 dst_sel:DWORD dst_unused:UNUSED_PAD src0_sel:WORD_1
	v_pk_fma_f32 v[20:21], v[4:5], v[12:13], v[20:21] op_sel:[0,1,0] op_sel_hi:[1,0,1]
	v_cvt_f32_f16_e32 v84, v71
	v_pk_fma_f32 v[12:13], v[10:11], v[12:13], v[20:21]
	v_cvt_f32_f16_sdwa v85, v71 dst_sel:DWORD dst_unused:UNUSED_PAD src0_sel:WORD_1
	v_pk_fma_f32 v[22:23], v[4:5], v[12:13], v[22:23] op_sel:[0,1,0] op_sel_hi:[1,0,1]
	v_cvt_f32_f16_e32 v86, v72
	v_pk_fma_f32 v[12:13], v[10:11], v[12:13], v[22:23]
	v_cvt_f32_f16_sdwa v87, v72 dst_sel:DWORD dst_unused:UNUSED_PAD src0_sel:WORD_1
	v_pk_fma_f32 v[24:25], v[4:5], v[12:13], v[24:25] op_sel:[0,1,0] op_sel_hi:[1,0,1]
	v_cvt_f32_f16_e32 v88, v73
	v_pk_fma_f32 v[12:13], v[10:11], v[12:13], v[24:25]
	v_cvt_f32_f16_sdwa v89, v73 dst_sel:DWORD dst_unused:UNUSED_PAD src0_sel:WORD_1
	ds_read2_b32 v[66:67], v30 offset1:96
	ds_read2_b32 v[68:69], v31 offset0:64 offset1:160
	ds_read2_b32 v[70:71], v32 offset1:96
	ds_read2_b32 v[72:73], v33 offset0:64 offset1:160
	v_add_u32_e32 v30, 0x1800, v30
	v_add_u32_e32 v31, 0x1800, v31
	v_add_u32_e32 v32, 0x1800, v32
	v_add_u32_e32 v33, 0x1800, v33
	s_waitcnt lgkmcnt(8)
	v_pk_fma_f32 v[74:75], v[4:5], v[12:13], v[74:75] op_sel:[0,1,0] op_sel_hi:[1,0,1]
	v_cvt_f32_f16_e32 v90, v50
	v_pk_fma_f32 v[12:13], v[10:11], v[12:13], v[74:75]
	v_cvt_f32_f16_sdwa v91, v50 dst_sel:DWORD dst_unused:UNUSED_PAD src0_sel:WORD_1
	v_pk_fma_f32 v[76:77], v[4:5], v[12:13], v[76:77] op_sel:[0,1,0] op_sel_hi:[1,0,1]
	v_cvt_f32_f16_e32 v92, v51
	v_pk_fma_f32 v[12:13], v[10:11], v[12:13], v[76:77]
	v_cvt_f32_f16_sdwa v93, v51 dst_sel:DWORD dst_unused:UNUSED_PAD src0_sel:WORD_1
	v_pk_fma_f32 v[78:79], v[4:5], v[12:13], v[78:79] op_sel:[0,1,0] op_sel_hi:[1,0,1]
	v_cvt_f32_f16_e32 v94, v52
	v_pk_fma_f32 v[12:13], v[10:11], v[12:13], v[78:79]
	v_cvt_f32_f16_sdwa v95, v52 dst_sel:DWORD dst_unused:UNUSED_PAD src0_sel:WORD_1
	v_pk_fma_f32 v[80:81], v[4:5], v[12:13], v[80:81] op_sel:[0,1,0] op_sel_hi:[1,0,1]
	v_cvt_f32_f16_e32 v96, v53
	v_pk_fma_f32 v[12:13], v[10:11], v[12:13], v[80:81]
	v_cvt_f32_f16_sdwa v97, v53 dst_sel:DWORD dst_unused:UNUSED_PAD src0_sel:WORD_1
	v_pk_fma_f32 v[82:83], v[4:5], v[12:13], v[82:83] op_sel:[0,1,0] op_sel_hi:[1,0,1]
	v_cvt_f32_f16_e32 v18, v54
	v_pk_fma_f32 v[12:13], v[10:11], v[12:13], v[82:83]
	v_cvt_f32_f16_sdwa v19, v54 dst_sel:DWORD dst_unused:UNUSED_PAD src0_sel:WORD_1
	v_pk_fma_f32 v[84:85], v[4:5], v[12:13], v[84:85] op_sel:[0,1,0] op_sel_hi:[1,0,1]
	v_cvt_f32_f16_e32 v20, v55
	v_pk_fma_f32 v[12:13], v[10:11], v[12:13], v[84:85]
	v_cvt_f32_f16_sdwa v21, v55 dst_sel:DWORD dst_unused:UNUSED_PAD src0_sel:WORD_1
	v_pk_fma_f32 v[86:87], v[4:5], v[12:13], v[86:87] op_sel:[0,1,0] op_sel_hi:[1,0,1]
	v_cvt_f32_f16_e32 v22, v56
	v_pk_fma_f32 v[12:13], v[10:11], v[12:13], v[86:87]
	v_cvt_f32_f16_sdwa v23, v56 dst_sel:DWORD dst_unused:UNUSED_PAD src0_sel:WORD_1
	v_pk_fma_f32 v[88:89], v[4:5], v[12:13], v[88:89] op_sel:[0,1,0] op_sel_hi:[1,0,1]
	v_cvt_f32_f16_e32 v24, v57
	v_pk_fma_f32 v[12:13], v[10:11], v[12:13], v[88:89]
	v_cvt_f32_f16_sdwa v25, v57 dst_sel:DWORD dst_unused:UNUSED_PAD src0_sel:WORD_1
	ds_read2_b32 v[50:51], v26 offset1:96
	ds_read2_b32 v[52:53], v27 offset0:64 offset1:160
	ds_read2_b32 v[54:55], v28 offset1:96
	ds_read2_b32 v[56:57], v29 offset0:64 offset1:160
	v_add_u32_e32 v26, 0x1800, v26
	v_add_u32_e32 v27, 0x1800, v27
	v_add_u32_e32 v28, 0x1800, v28
	v_add_u32_e32 v29, 0x1800, v29
	s_waitcnt lgkmcnt(8)
	v_pk_fma_f32 v[90:91], v[4:5], v[12:13], v[90:91] op_sel:[0,1,0] op_sel_hi:[1,0,1]
	v_cvt_f32_f16_e32 v74, v58
	v_pk_fma_f32 v[12:13], v[10:11], v[12:13], v[90:91]
	v_cvt_f32_f16_sdwa v75, v58 dst_sel:DWORD dst_unused:UNUSED_PAD src0_sel:WORD_1
	v_pk_fma_f32 v[92:93], v[4:5], v[12:13], v[92:93] op_sel:[0,1,0] op_sel_hi:[1,0,1]
	v_cvt_f32_f16_e32 v76, v59
	v_pk_fma_f32 v[12:13], v[10:11], v[12:13], v[92:93]
	v_cvt_f32_f16_sdwa v77, v59 dst_sel:DWORD dst_unused:UNUSED_PAD src0_sel:WORD_1
	v_pk_fma_f32 v[94:95], v[4:5], v[12:13], v[94:95] op_sel:[0,1,0] op_sel_hi:[1,0,1]
	v_cvt_f32_f16_e32 v78, v60
	v_pk_fma_f32 v[12:13], v[10:11], v[12:13], v[94:95]
	v_cvt_f32_f16_sdwa v79, v60 dst_sel:DWORD dst_unused:UNUSED_PAD src0_sel:WORD_1
	v_pk_fma_f32 v[96:97], v[4:5], v[12:13], v[96:97] op_sel:[0,1,0] op_sel_hi:[1,0,1]
	v_cvt_f32_f16_e32 v80, v61
	v_pk_fma_f32 v[12:13], v[10:11], v[12:13], v[96:97]
	v_cvt_f32_f16_sdwa v81, v61 dst_sel:DWORD dst_unused:UNUSED_PAD src0_sel:WORD_1
	v_pk_fma_f32 v[18:19], v[4:5], v[12:13], v[18:19] op_sel:[0,1,0] op_sel_hi:[1,0,1]
	v_cvt_f32_f16_e32 v82, v62
	v_pk_fma_f32 v[12:13], v[10:11], v[12:13], v[18:19]
	v_cvt_f32_f16_sdwa v83, v62 dst_sel:DWORD dst_unused:UNUSED_PAD src0_sel:WORD_1
	v_pk_fma_f32 v[20:21], v[4:5], v[12:13], v[20:21] op_sel:[0,1,0] op_sel_hi:[1,0,1]
	v_cvt_f32_f16_e32 v84, v63
	v_pk_fma_f32 v[12:13], v[10:11], v[12:13], v[20:21]
	v_cvt_f32_f16_sdwa v85, v63 dst_sel:DWORD dst_unused:UNUSED_PAD src0_sel:WORD_1
	v_pk_fma_f32 v[22:23], v[4:5], v[12:13], v[22:23] op_sel:[0,1,0] op_sel_hi:[1,0,1]
	v_cvt_f32_f16_e32 v86, v64
	v_pk_fma_f32 v[12:13], v[10:11], v[12:13], v[22:23]
	v_cvt_f32_f16_sdwa v87, v64 dst_sel:DWORD dst_unused:UNUSED_PAD src0_sel:WORD_1
	v_pk_fma_f32 v[24:25], v[4:5], v[12:13], v[24:25] op_sel:[0,1,0] op_sel_hi:[1,0,1]
	v_cvt_f32_f16_e32 v88, v65
	v_pk_fma_f32 v[12:13], v[10:11], v[12:13], v[24:25]
	v_cvt_f32_f16_sdwa v89, v65 dst_sel:DWORD dst_unused:UNUSED_PAD src0_sel:WORD_1
	ds_read2_b32 v[58:59], v30 offset1:96
	ds_read2_b32 v[60:61], v31 offset0:64 offset1:160
	ds_read2_b32 v[62:63], v32 offset1:96
	ds_read2_b32 v[64:65], v33 offset0:64 offset1:160
	v_add_u32_e32 v30, 0x1800, v30
	v_add_u32_e32 v31, 0x1800, v31
	v_add_u32_e32 v32, 0x1800, v32
	v_add_u32_e32 v33, 0x1800, v33
	s_waitcnt lgkmcnt(8)
	v_pk_fma_f32 v[74:75], v[4:5], v[12:13], v[74:75] op_sel:[0,1,0] op_sel_hi:[1,0,1]
	v_cvt_f32_f16_e32 v90, v66
	v_pk_fma_f32 v[12:13], v[10:11], v[12:13], v[74:75]
	v_cvt_f32_f16_sdwa v91, v66 dst_sel:DWORD dst_unused:UNUSED_PAD src0_sel:WORD_1
	v_pk_fma_f32 v[76:77], v[4:5], v[12:13], v[76:77] op_sel:[0,1,0] op_sel_hi:[1,0,1]
	v_cvt_f32_f16_e32 v92, v67
	v_pk_fma_f32 v[12:13], v[10:11], v[12:13], v[76:77]
	v_cvt_f32_f16_sdwa v93, v67 dst_sel:DWORD dst_unused:UNUSED_PAD src0_sel:WORD_1
	v_pk_fma_f32 v[78:79], v[4:5], v[12:13], v[78:79] op_sel:[0,1,0] op_sel_hi:[1,0,1]
	v_cvt_f32_f16_e32 v94, v68
	v_pk_fma_f32 v[12:13], v[10:11], v[12:13], v[78:79]
	v_cvt_f32_f16_sdwa v95, v68 dst_sel:DWORD dst_unused:UNUSED_PAD src0_sel:WORD_1
	v_pk_fma_f32 v[80:81], v[4:5], v[12:13], v[80:81] op_sel:[0,1,0] op_sel_hi:[1,0,1]
	v_cvt_f32_f16_e32 v96, v69
	v_pk_fma_f32 v[12:13], v[10:11], v[12:13], v[80:81]
	v_cvt_f32_f16_sdwa v97, v69 dst_sel:DWORD dst_unused:UNUSED_PAD src0_sel:WORD_1
	v_pk_fma_f32 v[82:83], v[4:5], v[12:13], v[82:83] op_sel:[0,1,0] op_sel_hi:[1,0,1]
	v_cvt_f32_f16_e32 v18, v70
	v_pk_fma_f32 v[12:13], v[10:11], v[12:13], v[82:83]
	v_cvt_f32_f16_sdwa v19, v70 dst_sel:DWORD dst_unused:UNUSED_PAD src0_sel:WORD_1
	v_pk_fma_f32 v[84:85], v[4:5], v[12:13], v[84:85] op_sel:[0,1,0] op_sel_hi:[1,0,1]
	v_cvt_f32_f16_e32 v20, v71
	v_pk_fma_f32 v[12:13], v[10:11], v[12:13], v[84:85]
	v_cvt_f32_f16_sdwa v21, v71 dst_sel:DWORD dst_unused:UNUSED_PAD src0_sel:WORD_1
	v_pk_fma_f32 v[86:87], v[4:5], v[12:13], v[86:87] op_sel:[0,1,0] op_sel_hi:[1,0,1]
	v_cvt_f32_f16_e32 v22, v72
	v_pk_fma_f32 v[12:13], v[10:11], v[12:13], v[86:87]
	v_cvt_f32_f16_sdwa v23, v72 dst_sel:DWORD dst_unused:UNUSED_PAD src0_sel:WORD_1
	v_pk_fma_f32 v[88:89], v[4:5], v[12:13], v[88:89] op_sel:[0,1,0] op_sel_hi:[1,0,1]
	v_cvt_f32_f16_e32 v24, v73
	v_pk_fma_f32 v[12:13], v[10:11], v[12:13], v[88:89]
	v_cvt_f32_f16_sdwa v25, v73 dst_sel:DWORD dst_unused:UNUSED_PAD src0_sel:WORD_1
	s_waitcnt lgkmcnt(4)
	v_pk_fma_f32 v[90:91], v[4:5], v[12:13], v[90:91] op_sel:[0,1,0] op_sel_hi:[1,0,1]
	v_cvt_f32_f16_e32 v74, v50
	v_pk_fma_f32 v[12:13], v[10:11], v[12:13], v[90:91]
	v_cvt_f32_f16_sdwa v75, v50 dst_sel:DWORD dst_unused:UNUSED_PAD src0_sel:WORD_1
	v_pk_fma_f32 v[92:93], v[4:5], v[12:13], v[92:93] op_sel:[0,1,0] op_sel_hi:[1,0,1]
	v_cvt_f32_f16_e32 v76, v51
	v_pk_fma_f32 v[12:13], v[10:11], v[12:13], v[92:93]
	v_cvt_f32_f16_sdwa v77, v51 dst_sel:DWORD dst_unused:UNUSED_PAD src0_sel:WORD_1
	v_pk_fma_f32 v[94:95], v[4:5], v[12:13], v[94:95] op_sel:[0,1,0] op_sel_hi:[1,0,1]
	v_cvt_f32_f16_e32 v78, v52
	v_pk_fma_f32 v[12:13], v[10:11], v[12:13], v[94:95]
	v_cvt_f32_f16_sdwa v79, v52 dst_sel:DWORD dst_unused:UNUSED_PAD src0_sel:WORD_1
	v_pk_fma_f32 v[96:97], v[4:5], v[12:13], v[96:97] op_sel:[0,1,0] op_sel_hi:[1,0,1]
	v_cvt_f32_f16_e32 v80, v53
	v_pk_fma_f32 v[12:13], v[10:11], v[12:13], v[96:97]
	v_cvt_f32_f16_sdwa v81, v53 dst_sel:DWORD dst_unused:UNUSED_PAD src0_sel:WORD_1
	v_pk_fma_f32 v[18:19], v[4:5], v[12:13], v[18:19] op_sel:[0,1,0] op_sel_hi:[1,0,1]
	v_cvt_f32_f16_e32 v82, v54
	v_pk_fma_f32 v[12:13], v[10:11], v[12:13], v[18:19]
	v_cvt_f32_f16_sdwa v83, v54 dst_sel:DWORD dst_unused:UNUSED_PAD src0_sel:WORD_1
	v_pk_fma_f32 v[20:21], v[4:5], v[12:13], v[20:21] op_sel:[0,1,0] op_sel_hi:[1,0,1]
	v_cvt_f32_f16_e32 v84, v55
	v_pk_fma_f32 v[12:13], v[10:11], v[12:13], v[20:21]
	v_cvt_f32_f16_sdwa v85, v55 dst_sel:DWORD dst_unused:UNUSED_PAD src0_sel:WORD_1
	v_pk_fma_f32 v[22:23], v[4:5], v[12:13], v[22:23] op_sel:[0,1,0] op_sel_hi:[1,0,1]
	v_cvt_f32_f16_e32 v86, v56
	v_pk_fma_f32 v[12:13], v[10:11], v[12:13], v[22:23]
	v_cvt_f32_f16_sdwa v87, v56 dst_sel:DWORD dst_unused:UNUSED_PAD src0_sel:WORD_1
	v_pk_fma_f32 v[24:25], v[4:5], v[12:13], v[24:25] op_sel:[0,1,0] op_sel_hi:[1,0,1]
	v_cvt_f32_f16_e32 v88, v57
	v_pk_fma_f32 v[12:13], v[10:11], v[12:13], v[24:25]
	v_cvt_f32_f16_sdwa v89, v57 dst_sel:DWORD dst_unused:UNUSED_PAD src0_sel:WORD_1
	s_waitcnt lgkmcnt(0)
	v_pk_fma_f32 v[74:75], v[4:5], v[12:13], v[74:75] op_sel:[0,1,0] op_sel_hi:[1,0,1]
	v_cvt_f32_f16_e32 v90, v58
	v_pk_fma_f32 v[12:13], v[10:11], v[12:13], v[74:75]
	v_cvt_f32_f16_sdwa v91, v58 dst_sel:DWORD dst_unused:UNUSED_PAD src0_sel:WORD_1
	v_pk_fma_f32 v[76:77], v[4:5], v[12:13], v[76:77] op_sel:[0,1,0] op_sel_hi:[1,0,1]
	v_cvt_f32_f16_e32 v92, v59
	v_pk_fma_f32 v[12:13], v[10:11], v[12:13], v[76:77]
	v_cvt_f32_f16_sdwa v93, v59 dst_sel:DWORD dst_unused:UNUSED_PAD src0_sel:WORD_1
	v_pk_fma_f32 v[78:79], v[4:5], v[12:13], v[78:79] op_sel:[0,1,0] op_sel_hi:[1,0,1]
	v_cvt_f32_f16_e32 v94, v60
	v_pk_fma_f32 v[12:13], v[10:11], v[12:13], v[78:79]
	v_cvt_f32_f16_sdwa v95, v60 dst_sel:DWORD dst_unused:UNUSED_PAD src0_sel:WORD_1
	v_pk_fma_f32 v[80:81], v[4:5], v[12:13], v[80:81] op_sel:[0,1,0] op_sel_hi:[1,0,1]
	v_cvt_f32_f16_e32 v96, v61
	v_pk_fma_f32 v[12:13], v[10:11], v[12:13], v[80:81]
	v_cvt_f32_f16_sdwa v97, v61 dst_sel:DWORD dst_unused:UNUSED_PAD src0_sel:WORD_1
	v_pk_fma_f32 v[82:83], v[4:5], v[12:13], v[82:83] op_sel:[0,1,0] op_sel_hi:[1,0,1]
	v_cvt_f32_f16_e32 v18, v62
	v_pk_fma_f32 v[12:13], v[10:11], v[12:13], v[82:83]
	v_cvt_f32_f16_sdwa v19, v62 dst_sel:DWORD dst_unused:UNUSED_PAD src0_sel:WORD_1
	v_pk_fma_f32 v[84:85], v[4:5], v[12:13], v[84:85] op_sel:[0,1,0] op_sel_hi:[1,0,1]
	v_cvt_f32_f16_e32 v20, v63
	v_pk_fma_f32 v[12:13], v[10:11], v[12:13], v[84:85]
	v_cvt_f32_f16_sdwa v21, v63 dst_sel:DWORD dst_unused:UNUSED_PAD src0_sel:WORD_1
	v_pk_fma_f32 v[86:87], v[4:5], v[12:13], v[86:87] op_sel:[0,1,0] op_sel_hi:[1,0,1]
	v_cvt_f32_f16_e32 v22, v64
	v_pk_fma_f32 v[12:13], v[10:11], v[12:13], v[86:87]
	v_cvt_f32_f16_sdwa v23, v64 dst_sel:DWORD dst_unused:UNUSED_PAD src0_sel:WORD_1
	v_pk_fma_f32 v[88:89], v[4:5], v[12:13], v[88:89] op_sel:[0,1,0] op_sel_hi:[1,0,1]
	v_cvt_f32_f16_e32 v24, v65
	v_pk_fma_f32 v[12:13], v[10:11], v[12:13], v[88:89]
	v_cvt_f32_f16_sdwa v25, v65 dst_sel:DWORD dst_unused:UNUSED_PAD src0_sel:WORD_1
	v_pk_fma_f32 v[90:91], v[4:5], v[12:13], v[90:91] op_sel:[0,1,0] op_sel_hi:[1,0,1]
	s_nop 0
	v_pk_fma_f32 v[12:13], v[10:11], v[12:13], v[90:91]
	s_nop 0
	v_pk_fma_f32 v[92:93], v[4:5], v[12:13], v[92:93] op_sel:[0,1,0] op_sel_hi:[1,0,1]
	s_nop 0
	v_pk_fma_f32 v[12:13], v[10:11], v[12:13], v[92:93]
	s_nop 0
	v_pk_fma_f32 v[94:95], v[4:5], v[12:13], v[94:95] op_sel:[0,1,0] op_sel_hi:[1,0,1]
	s_nop 0
	v_pk_fma_f32 v[12:13], v[10:11], v[12:13], v[94:95]
	s_nop 0
	v_pk_fma_f32 v[96:97], v[4:5], v[12:13], v[96:97] op_sel:[0,1,0] op_sel_hi:[1,0,1]
	s_nop 0
	v_pk_fma_f32 v[12:13], v[10:11], v[12:13], v[96:97]
	s_nop 0
	v_pk_fma_f32 v[18:19], v[4:5], v[12:13], v[18:19] op_sel:[0,1,0] op_sel_hi:[1,0,1]
	s_nop 0
	v_pk_fma_f32 v[12:13], v[10:11], v[12:13], v[18:19]
	s_nop 0
	v_pk_fma_f32 v[20:21], v[4:5], v[12:13], v[20:21] op_sel:[0,1,0] op_sel_hi:[1,0,1]
	s_nop 0
	v_pk_fma_f32 v[12:13], v[10:11], v[12:13], v[20:21]
	s_nop 0
	v_pk_fma_f32 v[22:23], v[4:5], v[12:13], v[22:23] op_sel:[0,1,0] op_sel_hi:[1,0,1]
	s_nop 0
	v_pk_fma_f32 v[12:13], v[10:11], v[12:13], v[22:23]
	s_nop 0
	v_pk_fma_f32 v[24:25], v[4:5], v[12:13], v[24:25] op_sel:[0,1,0] op_sel_hi:[1,0,1]
	s_nop 0
	v_pk_fma_f32 v[12:13], v[10:11], v[12:13], v[24:25]
	s_nop 0
	v_mul_lo_u32 v4, v49, s67
	v_lshlrev_b32_e32 v5, 3, v14
	v_readlane_b32 s4, v230, 8
	s_nop 1
	v_add3_u32 v4, s4, v4, v5
	ds_write_b64 v4, v[12:13]
	v_mov_b32_e32 v4, v2
.LBB1_73:
	s_or_b64 exec, exec, s[0:1]
	s_movk_i32 s0, 0x60
	v_cmp_gt_i32_e64 s[0:1], s0, v107
	v_lshl_add_u32 v5, v14, 3, 0
	s_waitcnt lgkmcnt(0)
	s_barrier
	s_and_saveexec_b64 s[98:99], s[0:1]
	s_cbranch_execz .LBB1_195
	v_add_u32_e32 v2, 0x18000, v5
	ds_read2_b64 v[10:13], v2 offset1:96
	v_add_u32_e32 v2, 0x400, v2
	ds_read2_b64 v[14:17], v2 offset0:64 offset1:160
	v_readlane_b32 s4, v230, 2
	v_readlane_b32 s6, v230, 4
	s_waitcnt vmcnt(0) lgkmcnt(1)
	v_fmamk_f32 v10, v7, 0x80000000, v10
	v_fmac_f32_e32 v10, 0, v6
	v_fma_f32 v11, 0, v7, v11
	v_fmac_f32_e32 v11, 0, v6
	v_fmac_f32_e32 v13, v7, v10
	v_fma_f32 v12, -v7, v11, v12
	v_fmac_f32_e32 v13, v6, v11
	v_fmac_f32_e32 v12, v6, v10
	s_waitcnt lgkmcnt(0)
	v_fma_f32 v2, -v7, v13, v14
	v_fmac_f32_e32 v2, v6, v12
	v_fma_f32 v10, v7, v12, v15
	v_fmac_f32_e32 v10, v6, v13
	v_fmac_f32_e32 v17, v7, v2
	v_readlane_b32 s7, v230, 5
	v_fma_f32 v16, -v7, v10, v16
	v_fmac_f32_e32 v17, v6, v10
	v_mov_b64_e32 v[10:11], s[6:7]
	v_mad_i64_i32 v[10:11], s[0:1], v98, s62, v[10:11]
	v_lshlrev_b64 v[8:9], 3, v[8:9]
	v_fmac_f32_e32 v16, v6, v2
	v_and_b32_e32 v13, -16, v98
	v_lshl_add_u64 v[10:11], v[10:11], 0, v[8:9]
	v_lshl_add_u64 v[8:9], s[6:7], 0, v[8:9]
	global_store_dwordx2 v[10:11], v[16:17], off sc1
	v_subrev_u32_e32 v42, s6, v8
	v_mul_u32_u24_e32 v43, 0xc00, v13
	v_add_u32_e32 v42, v42, v43
	v_mov_b32_e32 v40, v182
	v_mov_b32_e32 v41, v183
	v_mov_b32_e32 v38, v184
	v_mov_b32_e32 v39, v185
	v_mov_b32_e32 v36, v186
	v_mov_b32_e32 v37, v187
	v_mov_b32_e32 v34, v188
	v_mov_b32_e32 v35, v189
	v_mov_b32_e32 v32, v190
	v_mov_b32_e32 v33, v191
	v_mov_b32_e32 v30, v192
	v_mov_b32_e32 v31, v193
	v_mov_b32_e32 v28, v194
	v_mov_b32_e32 v29, v195
	v_mov_b32_e32 v26, v196
	v_mov_b32_e32 v27, v197
	v_mov_b32_e32 v24, v198
	v_mov_b32_e32 v25, v199
	v_mov_b32_e32 v22, v200
	v_mov_b32_e32 v23, v201
	v_mov_b32_e32 v20, v202
	v_mov_b32_e32 v21, v203
	v_mov_b32_e32 v18, v204
	v_mov_b32_e32 v19, v205
	v_mov_b32_e32 v16, v206
	v_mov_b32_e32 v17, v207
	v_mov_b32_e32 v14, v208
	v_mov_b32_e32 v15, v209
	v_mov_b32_e32 v10, v210
	v_mov_b32_e32 v11, v211
	v_cmp_ne_u32_e64 s[30:31], 0, v122
	v_cmp_lt_u32_e64 s[28:29], 1, v122
	v_cmp_lt_u32_e64 s[26:27], 2, v122
	v_cmp_lt_u32_e64 s[24:25], 4, v122
	v_cmp_lt_u32_e64 s[22:23], 5, v122
	v_cmp_lt_u32_e64 s[20:21], 6, v122
	v_cmp_lt_u32_e64 s[18:19], 7, v122
	v_cmp_lt_u32_e64 s[16:17], 8, v122
	v_cmp_lt_u32_e64 s[14:15], 9, v122
	v_cmp_lt_u32_e64 s[12:13], 10, v122
	v_cmp_lt_u32_e64 s[10:11], 11, v122
	v_cmp_lt_u32_e64 s[8:9], 12, v122
	v_cmp_lt_u32_e64 s[6:7], 13, v122
	v_cmp_eq_u32_e64 s[4:5], 15, v122
	v_pk_mul_f32 v[42:43], v[6:7], v[6:7]
	v_add_f32_e32 v12, v6, v6
	v_sub_f32_e32 v2, v42, v43
	v_mul_f32_e32 v12, v7, v12
	v_add_f32_e32 v42, v2, v2
	v_mul_f32_e32 v2, v2, v2
	v_mov_b32_e32 v108, v109
	v_fma_f32 v2, -v12, v12, v2
	v_mul_f32_e32 v12, v12, v42
	v_mov_b64_e32 v[42:43], v[108:109]
	s_and_saveexec_b64 s[72:73], s[30:31]
	s_cbranch_execnz .LBB1_119
	s_or_b64 exec, exec, s[72:73]
	s_and_saveexec_b64 s[30:31], s[28:29]
	s_cbranch_execnz .LBB1_124
